# P4 first-branch epilogue (Lever 2): second row-half's 8 gate loads issued with the first half's into free registers, first wait vmcnt(8), copies at the old load sites; on top of the no-copy version
# speedup vs baseline: 1.0100x; 1.0100x over previous
.LBB0_995:
	v_lshl_or_b32 v2, s41, 8, v198
	v_ashrrev_i32_e32 v3, 31, v2
	v_readlane_b32 s24, v255, 4
	v_lshlrev_b64 v[10:11], 1, v[2:3]
	v_readlane_b32 s25, v255, 5
	v_lshl_add_u32 v180, s20, 8, v196
	s_nop 15
	s_nop 15
	v_or_b32_e32 v203, 16, v180
	v_lshl_add_u64 v[14:15], s[24:25], 0, v[10:11]
	v_mad_i64_i32 v[2:3], s[22:23], v180, s38, v[14:15]
	v_add_co_u32_e32 v2, vcc, 0x7000, v2
	v_mov_b64_e32 v[12:13], s[24:25]
	s_nop 0
	v_addc_co_u32_e32 v3, vcc, 0, v3, vcc
	global_load_dwordx4 v[16:19], v[2:3], off nt
	global_load_dwordx4 v[20:23], v[2:3], off offset:256 nt
	v_mad_i64_i32 v[2:3], s[22:23], v203, s38, v[14:15]
	v_add_co_u32_e32 v2, vcc, 0x7000, v2
	v_mad_i64_i32 v[4:5], s[22:23], v180, s38, v[12:13]
	s_nop 0
	v_addc_co_u32_e32 v3, vcc, 0, v3, vcc
	global_load_dwordx4 v[24:27], v[2:3], off nt
	global_load_dwordx4 v[28:31], v[2:3], off offset:256 nt
	v_lshl_add_u64 v[4:5], v[4:5], 0, v[10:11]
	v_or_b32_e32 v204, 32, v180
	v_add_co_u32_e32 v32, vcc, s40, v4
	v_mad_i64_i32 v[6:7], s[22:23], v204, s38, v[14:15]
	s_nop 0
	v_addc_co_u32_e32 v33, vcc, 0, v5, vcc
	v_add_co_u32_e32 v4, vcc, 0x7000, v6
	v_mul_f32_e32 v181, 0x3d000000, v150
	s_nop 0
	v_addc_co_u32_e32 v5, vcc, 0, v7, vcc
	v_mul_f32_e32 v182, 0x3d000000, v146
	v_mul_f32_e32 v183, 0x3d000000, v151
	v_mul_f32_e32 v184, 0x3d000000, v147
	v_mul_f32_e32 v185, 0x3d000000, v152
	v_mul_f32_e32 v186, 0x3d000000, v148
	v_mul_f32_e32 v187, 0x3d000000, v153
	v_mul_f32_e32 v202, 0x3d000000, v149
	global_load_dwordx4 v[146:149], v[4:5], off nt
	global_load_dwordx4 v[150:153], v[4:5], off offset:256 nt
	v_or_b32_e32 v205, 48, v180
	v_mad_i64_i32 v[8:9], s[22:23], v205, s38, v[14:15]
	v_add_co_u32_e32 v2, vcc, 0x7000, v8
	v_mul_f32_e32 v161, 0x3d000000, v161
	s_nop 0
	v_addc_co_u32_e32 v3, vcc, 0, v9, vcc
	global_load_dwordx4 v[6:9], v[2:3], off nt
	s_nop 0
	global_load_dwordx4 v[2:5], v[2:3], off offset:256 nt
	v_add_u32_e32 v246, 0x80, v180
	v_mad_i64_i32 v[248:249], s[22:23], v246, s38, v[14:15]
	v_add_co_u32_e32 v248, vcc, s39, v248
	s_nop 1
	v_addc_co_u32_e32 v249, vcc, 0, v249, vcc
	global_load_dwordx4 v[214:217], v[248:249], off nt
	global_load_dwordx4 v[218:221], v[248:249], off offset:256 nt
	v_add_u32_e32 v246, 0x90, v180
	v_mad_i64_i32 v[248:249], s[22:23], v246, s38, v[14:15]
	v_add_co_u32_e32 v248, vcc, s39, v248
	s_nop 1
	v_addc_co_u32_e32 v249, vcc, 0, v249, vcc
	global_load_dwordx4 v[222:225], v[248:249], off nt
	global_load_dwordx4 v[226:229], v[248:249], off offset:256 nt
	v_add_u32_e32 v246, 0xa0, v180
	v_mad_i64_i32 v[248:249], s[22:23], v246, s38, v[14:15]
	v_add_co_u32_e32 v248, vcc, s39, v248
	s_nop 1
	v_addc_co_u32_e32 v249, vcc, 0, v249, vcc
	global_load_dwordx4 v[230:233], v[248:249], off nt
	global_load_dwordx4 v[234:237], v[248:249], off offset:256 nt
	v_add_u32_e32 v246, 0xb0, v180
	v_mad_i64_i32 v[248:249], s[22:23], v246, s38, v[14:15]
	v_add_co_u32_e32 v248, vcc, s39, v248
	s_nop 1
	v_addc_co_u32_e32 v249, vcc, 0, v249, vcc
	global_load_dwordx4 v[238:241], v[248:249], off nt
	global_load_dwordx4 v[242:245], v[248:249], off offset:256 nt
	v_mul_f32_e32 v159, 0x3d000000, v159
	v_mul_f32_e32 v155, 0x3d000000, v155
	v_mul_f32_e32 v160, 0x3d000000, v160
	v_mul_f32_e32 v157, 0x3d000000, v157
	v_mul_f32_e32 v158, 0x3d000000, v158
	v_mul_f32_e32 v154, 0x3d000000, v154
	v_mul_f32_e32 v156, 0x3d000000, v156
	v_mul_f32_e32 v94, 0x3d000000, v94
	v_mul_f32_e32 v95, 0x3d000000, v95
	v_mul_f32_e32 v91, 0x3d000000, v91
	v_mul_f32_e32 v96, 0x3d000000, v96
	v_mul_f32_e32 v90, 0x3d000000, v90
	v_mul_f32_e32 v97, 0x3d000000, v97
	v_mul_f32_e32 v93, 0x3d000000, v93
	v_mul_f32_e32 v92, 0x3d000000, v92
	s_waitcnt vmcnt(8)
	v_lshlrev_b32_e32 v207, 16, v17
	v_and_b32_e32 v17, 0xffff0000, v17
	v_lshlrev_b32_e32 v206, 16, v16
	v_and_b32_e32 v16, 0xffff0000, v16
	v_lshlrev_b32_e32 v208, 16, v18
	v_and_b32_e32 v18, 0xffff0000, v18
	v_lshlrev_b32_e32 v209, 16, v19
	v_and_b32_e32 v19, 0xffff0000, v19
	v_mul_f32_e32 v17, v161, v17
	v_mul_f32_e32 v16, v159, v16
	v_mul_f32_e32 v159, v160, v207
	v_mul_f32_e32 v18, v155, v18
	v_mul_f32_e32 v19, v157, v19
	v_cvt_pk_bf16_f32 v17, v159, v17
	v_lshlrev_b32_e32 v210, 16, v20
	v_mul_f32_e32 v158, v158, v206
	v_mul_f32_e32 v154, v154, v208
	v_mul_f32_e32 v155, v156, v209
	v_cvt_pk_bf16_f32 v16, v158, v16
	v_cvt_pk_bf16_f32 v18, v154, v18
	v_cvt_pk_bf16_f32 v19, v155, v19
	global_store_dwordx4 v[32:33], v[16:19], off
	s_nop 1
	v_and_b32_e32 v17, 0xffff0000, v20
	v_mul_f32_e32 v16, v181, v210
	v_mul_f32_e32 v17, v183, v17
	v_lshlrev_b32_e32 v18, 16, v21
	v_and_b32_e32 v19, 0xffff0000, v21
	v_mul_f32_e32 v18, v185, v18
	v_mul_f32_e32 v19, v187, v19
	v_lshlrev_b32_e32 v20, 16, v22
	v_and_b32_e32 v21, 0xffff0000, v22
	v_lshlrev_b32_e32 v22, 16, v23
	v_and_b32_e32 v23, 0xffff0000, v23
	v_cvt_pk_bf16_f32 v16, v16, v17
	v_cvt_pk_bf16_f32 v17, v18, v19
	v_mul_f32_e32 v20, v182, v20
	v_mul_f32_e32 v21, v184, v21
	v_mul_f32_e32 v22, v186, v22
	v_mul_f32_e32 v23, v202, v23
	v_cvt_pk_bf16_f32 v18, v20, v21
	v_cvt_pk_bf16_f32 v19, v22, v23
	global_store_dwordx4 v[32:33], v[16:19], off offset:256
	v_mul_f32_e32 v22, 0x3d000000, v143
	v_mul_f32_e32 v23, 0x3d000000, v139
	v_mad_i64_i32 v[16:17], s[22:23], v203, s38, v[12:13]
	v_mul_f32_e32 v18, 0x3d000000, v142
	v_mul_f32_e32 v19, 0x3d000000, v138
	v_lshl_add_u64 v[20:21], v[16:17], 0, v[10:11]
	v_lshlrev_b32_e32 v16, 16, v24
	v_and_b32_e32 v17, 0xffff0000, v24
	v_lshlrev_b32_e32 v24, 16, v26
	v_mul_f32_e32 v32, 0x3d000000, v144
	v_mul_f32_e32 v16, v18, v16
	v_lshlrev_b32_e32 v18, 16, v25
	v_mul_f32_e32 v19, v19, v24
	v_and_b32_e32 v24, 0xffff0000, v26
	v_add_co_u32_e32 v20, vcc, s40, v20
	v_mul_f32_e32 v33, 0x3d000000, v140
	v_mul_f32_e32 v138, 0x3d000000, v145
	v_mul_f32_e32 v139, 0x3d000000, v141
	v_mul_f32_e32 v17, v22, v17
	v_mul_f32_e32 v18, v32, v18
	v_and_b32_e32 v22, 0xffff0000, v25
	v_mul_f32_e32 v23, v23, v24
	v_lshlrev_b32_e32 v24, 16, v27
	v_and_b32_e32 v25, 0xffff0000, v27
	v_cvt_pk_bf16_f32 v16, v16, v17
	v_addc_co_u32_e32 v21, vcc, 0, v21, vcc
	v_mul_f32_e32 v22, v138, v22
	v_mul_f32_e32 v24, v33, v24
	v_mul_f32_e32 v25, v139, v25
	v_cvt_pk_bf16_f32 v17, v18, v22
	v_cvt_pk_bf16_f32 v18, v19, v23
	v_cvt_pk_bf16_f32 v19, v24, v25
	global_store_dwordx4 v[20:21], v[16:19], off
	v_lshlrev_b32_e32 v26, 16, v28
	v_mul_f32_e32 v22, 0x3d000000, v136
	v_mul_f32_e32 v16, 0x3d000000, v134
	v_mul_f32_e32 v18, 0x3d000000, v135
	v_mul_f32_e32 v16, v16, v26
	v_and_b32_e32 v26, 0xffff0000, v28
	v_mul_f32_e32 v18, v18, v26
	v_lshlrev_b32_e32 v26, 16, v29
	v_mul_f32_e32 v24, 0x3d000000, v137
	v_mul_f32_e32 v22, v22, v26
	v_and_b32_e32 v26, 0xffff0000, v29
	v_mul_f32_e32 v17, 0x3d000000, v130
	v_mul_f32_e32 v24, v24, v26
	v_lshlrev_b32_e32 v26, 16, v30
	v_mul_f32_e32 v19, 0x3d000000, v131
	v_mul_f32_e32 v26, v17, v26
	v_and_b32_e32 v17, 0xffff0000, v30
	v_mul_f32_e32 v23, 0x3d000000, v132
	v_mul_f32_e32 v19, v19, v17
	v_lshlrev_b32_e32 v17, 16, v31
	v_mul_f32_e32 v25, 0x3d000000, v133
	v_mul_f32_e32 v23, v23, v17
	v_and_b32_e32 v17, 0xffff0000, v31
	v_mul_f32_e32 v25, v25, v17
	v_cvt_pk_bf16_f32 v16, v16, v18
	v_cvt_pk_bf16_f32 v17, v22, v24
	v_cvt_pk_bf16_f32 v18, v26, v19
	v_cvt_pk_bf16_f32 v19, v23, v25
	global_store_dwordx4 v[20:21], v[16:19], off offset:256
	v_mul_f32_e32 v24, 0x3d000000, v128
	v_mul_f32_e32 v23, 0x3d000000, v123
	v_mad_i64_i32 v[16:17], s[22:23], v204, s38, v[12:13]
	v_mul_f32_e32 v18, 0x3d000000, v126
	v_lshl_add_u64 v[20:21], v[16:17], 0, v[10:11]
	v_lshlrev_b32_e32 v16, 16, v146
	v_mul_f32_e32 v16, v18, v16
	v_lshlrev_b32_e32 v18, 16, v147
	v_mul_f32_e32 v19, 0x3d000000, v122
	v_mul_f32_e32 v18, v24, v18
	v_lshlrev_b32_e32 v24, 16, v148
	v_mul_f32_e32 v19, v19, v24
	v_and_b32_e32 v24, 0xffff0000, v148
	v_mul_f32_e32 v22, 0x3d000000, v127
	v_mul_f32_e32 v25, 0x3d000000, v124
	v_and_b32_e32 v17, 0xffff0000, v146
	v_mul_f32_e32 v23, v23, v24
	v_lshlrev_b32_e32 v24, 16, v149
	v_add_co_u32_e32 v20, vcc, s40, v20
	v_mul_f32_e32 v26, 0x3d000000, v129
	v_mul_f32_e32 v27, 0x3d000000, v125
	v_mul_f32_e32 v17, v22, v17
	v_and_b32_e32 v22, 0xffff0000, v147
	v_mul_f32_e32 v24, v25, v24
	v_and_b32_e32 v25, 0xffff0000, v149
	v_cvt_pk_bf16_f32 v16, v16, v17
	v_addc_co_u32_e32 v21, vcc, 0, v21, vcc
	v_mul_f32_e32 v22, v26, v22
	v_mul_f32_e32 v25, v27, v25
	v_cvt_pk_bf16_f32 v17, v18, v22
	v_cvt_pk_bf16_f32 v18, v19, v23
	v_cvt_pk_bf16_f32 v19, v24, v25
	global_store_dwordx4 v[20:21], v[16:19], off
	v_lshlrev_b32_e32 v26, 16, v150
	v_mul_f32_e32 v22, 0x3d000000, v120
	v_mul_f32_e32 v16, 0x3d000000, v118
	v_mul_f32_e32 v18, 0x3d000000, v119
	v_mul_f32_e32 v16, v16, v26
	v_and_b32_e32 v26, 0xffff0000, v150
	v_mul_f32_e32 v18, v18, v26
	v_lshlrev_b32_e32 v26, 16, v151
	v_mul_f32_e32 v24, 0x3d000000, v121
	v_mul_f32_e32 v22, v22, v26
	v_and_b32_e32 v26, 0xffff0000, v151
	v_mul_f32_e32 v17, 0x3d000000, v114
	v_mul_f32_e32 v24, v24, v26
	v_lshlrev_b32_e32 v26, 16, v152
	v_mul_f32_e32 v19, 0x3d000000, v115
	v_mul_f32_e32 v26, v17, v26
	v_and_b32_e32 v17, 0xffff0000, v152
	v_mul_f32_e32 v23, 0x3d000000, v116
	v_mul_f32_e32 v19, v19, v17
	v_lshlrev_b32_e32 v17, 16, v153
	v_mul_f32_e32 v25, 0x3d000000, v117
	v_mul_f32_e32 v23, v23, v17
	v_and_b32_e32 v17, 0xffff0000, v153
	v_mul_f32_e32 v25, v25, v17
	v_cvt_pk_bf16_f32 v16, v16, v18
	v_cvt_pk_bf16_f32 v17, v22, v24
	v_cvt_pk_bf16_f32 v18, v26, v19
	v_cvt_pk_bf16_f32 v19, v23, v25
	global_store_dwordx4 v[20:21], v[16:19], off offset:256
	v_mul_f32_e32 v22, 0x3d000000, v111
	v_mul_f32_e32 v24, 0x3d000000, v112
	v_mad_i64_i32 v[16:17], s[22:23], v205, s38, v[12:13]
	v_lshl_add_u64 v[20:21], v[16:17], 0, v[10:11]
	v_lshlrev_b32_e32 v16, 16, v6
	v_and_b32_e32 v6, 0xffff0000, v6
	v_mul_f32_e32 v29, v22, v6
	v_lshlrev_b32_e32 v6, 16, v7
	v_mul_f32_e32 v26, 0x3d000000, v113
	v_mul_f32_e32 v24, v24, v6
	v_and_b32_e32 v6, 0xffff0000, v7
	v_mul_f32_e32 v19, 0x3d000000, v106
	v_mul_f32_e32 v26, v26, v6
	v_lshlrev_b32_e32 v6, 16, v8
	v_mul_f32_e32 v23, 0x3d000000, v107
	v_mul_f32_e32 v30, v19, v6
	v_and_b32_e32 v6, 0xffff0000, v8
	v_mul_f32_e32 v25, 0x3d000000, v108
	v_mul_f32_e32 v8, v23, v6
	v_lshlrev_b32_e32 v6, 16, v9
	v_add_u32_e32 v32, 0x80, v180
	v_mul_f32_e32 v25, v25, v6
	v_mad_i64_i32 v[6:7], s[22:23], v32, s38, v[14:15]
	v_add_co_u32_e32 v22, vcc, s39, v6
	v_mul_f32_e32 v18, 0x3d000000, v110
	s_nop 0
	v_addc_co_u32_e32 v23, vcc, 0, v7, vcc
	v_mul_f32_e32 v27, 0x3d000000, v109
	v_mul_f32_e32 v28, v18, v16
	s_waitcnt vmcnt(6)
	v_mov_b64_e32 v[16:17], v[214:215]
	v_mov_b64_e32 v[18:19], v[216:217]
	v_and_b32_e32 v6, 0xffff0000, v9
	v_add_co_u32_e32 v20, vcc, s40, v20
	v_mul_f32_e32 v9, v27, v6
	v_cvt_pk_bf16_f32 v6, v28, v29
	s_nop 0
	v_addc_co_u32_e32 v21, vcc, 0, v21, vcc
	v_cvt_pk_bf16_f32 v7, v24, v26
	v_cvt_pk_bf16_f32 v8, v30, v8
	v_cvt_pk_bf16_f32 v9, v25, v9
	global_store_dwordx4 v[20:21], v[6:9], off
	v_lshlrev_b32_e32 v28, 16, v2
	v_mul_f32_e32 v24, 0x3d000000, v104
	v_mul_f32_e32 v6, 0x3d000000, v102
	v_mul_f32_e32 v28, v6, v28
	v_lshlrev_b32_e32 v6, 16, v3
	v_mul_f32_e32 v7, 0x3d000000, v98
	v_mul_f32_e32 v8, 0x3d000000, v103
	v_mul_f32_e32 v9, 0x3d000000, v99
	v_mul_f32_e32 v26, 0x3d000000, v105
	v_and_b32_e32 v2, 0xffff0000, v2
	v_mul_f32_e32 v24, v24, v6
	v_and_b32_e32 v3, 0xffff0000, v3
	v_lshlrev_b32_e32 v6, 16, v4
	v_and_b32_e32 v4, 0xffff0000, v4
	v_mul_f32_e32 v2, v8, v2
	v_mul_f32_e32 v3, v26, v3
	v_mul_f32_e32 v26, v7, v6
	v_mul_f32_e32 v4, v9, v4
	v_mov_b64_e32 v[6:7], v[218:219]
	v_mov_b64_e32 v[8:9], v[220:221]
	v_mul_f32_e32 v27, 0x3d000000, v101
	v_lshlrev_b32_e32 v29, 16, v5
	v_and_b32_e32 v5, 0xffff0000, v5
	v_mul_f32_e32 v25, 0x3d000000, v100
	v_mul_f32_e32 v5, v27, v5
	v_cvt_pk_bf16_f32 v2, v28, v2
	v_cvt_pk_bf16_f32 v3, v24, v3
	v_add_u32_e32 v106, 0x90, v180
	v_mul_f32_e32 v22, v25, v29
	v_cvt_pk_bf16_f32 v4, v26, v4
	v_cvt_pk_bf16_f32 v5, v22, v5
	global_store_dwordx4 v[20:21], v[2:5], off offset:256
	v_add_u32_e32 v107, 0xa0, v180
	v_add_u32_e32 v108, 0xb0, v180
	v_mad_i64_i32 v[2:3], s[22:23], v106, s38, v[14:15]
	v_add_co_u32_e32 v2, vcc, s39, v2
	s_nop 1
	v_addc_co_u32_e32 v3, vcc, 0, v3, vcc
	v_mov_b64_e32 v[20:21], v[222:223]
	v_mov_b64_e32 v[22:23], v[224:225]
	v_mov_b64_e32 v[24:25], v[226:227]
	v_mov_b64_e32 v[26:27], v[228:229]
	v_mad_i64_i32 v[2:3], s[22:23], v107, s38, v[14:15]
	v_add_co_u32_e32 v2, vcc, s39, v2
	s_nop 1
	v_addc_co_u32_e32 v3, vcc, 0, v3, vcc
	v_mov_b64_e32 v[28:29], v[230:231]
	v_mov_b64_e32 v[30:31], v[232:233]
	v_mov_b64_e32 v[98:99], v[234:235]
	v_mov_b64_e32 v[100:101], v[236:237]
	v_mad_i64_i32 v[2:3], s[22:23], v108, s38, v[14:15]
	v_add_co_u32_e32 v2, vcc, s39, v2
	v_mad_i64_i32 v[14:15], s[22:23], v32, s38, v[12:13]
	s_nop 0
	v_addc_co_u32_e32 v3, vcc, 0, v3, vcc
	v_mov_b64_e32 v[102:103], v[238:239]
	v_mov_b64_e32 v[104:105], v[240:241]
	s_nop 0
	v_mov_b64_e32 v[2:3], v[242:243]
	v_mov_b64_e32 v[4:5], v[244:245]
	v_lshl_add_u64 v[32:33], v[14:15], 0, v[10:11]
	v_lshlrev_b32_e32 v14, 16, v16
	v_mul_f32_e32 v14, v94, v14
	v_and_b32_e32 v15, 0xffff0000, v16
	v_lshlrev_b32_e32 v16, 16, v17
	v_lshlrev_b32_e32 v94, 16, v18
	v_and_b32_e32 v18, 0xffff0000, v18
	v_mul_f32_e32 v15, v95, v15
	v_mul_f32_e32 v16, v96, v16
	v_and_b32_e32 v17, 0xffff0000, v17
	v_mul_f32_e32 v18, v91, v18
	v_lshlrev_b32_e32 v91, 16, v19
	v_and_b32_e32 v19, 0xffff0000, v19
	v_mul_f32_e32 v17, v97, v17
	v_mul_f32_e32 v90, v90, v94
	v_mul_f32_e32 v19, v93, v19
	v_cvt_pk_bf16_f32 v14, v14, v15
	v_cvt_pk_bf16_f32 v15, v16, v17
	v_cvt_pk_bf16_f32 v16, v90, v18
	v_add_co_u32_e32 v18, vcc, s40, v32
	v_mul_f32_e32 v91, v92, v91
	v_cvt_pk_bf16_f32 v17, v91, v19
	s_nop 0
	v_addc_co_u32_e32 v19, vcc, 0, v33, vcc
	global_store_dwordx4 v[18:19], v[14:17], off
	v_mul_f32_e32 v33, 0x3d000000, v84
	v_mul_f32_e32 v32, 0x3d000000, v88
	v_mul_f32_e32 v16, 0x3d000000, v87
	v_mul_f32_e32 v15, 0x3d000000, v82
	v_mul_f32_e32 v17, 0x3d000000, v83
	v_lshlrev_b32_e32 v84, 16, v6
	v_and_b32_e32 v6, 0xffff0000, v6
	v_mul_f32_e32 v6, v16, v6
	v_lshlrev_b32_e32 v16, 16, v7
	v_mul_f32_e32 v82, 0x3d000000, v89
	v_mul_f32_e32 v16, v32, v16
	v_and_b32_e32 v7, 0xffff0000, v7
	v_lshlrev_b32_e32 v32, 16, v8
	v_and_b32_e32 v8, 0xffff0000, v8
	v_mul_f32_e32 v14, 0x3d000000, v86
	v_mul_f32_e32 v83, 0x3d000000, v85
	v_mul_f32_e32 v7, v82, v7
	v_mul_f32_e32 v8, v17, v8
	v_lshlrev_b32_e32 v17, 16, v9
	v_and_b32_e32 v9, 0xffff0000, v9
	v_mul_f32_e32 v14, v14, v84
	v_mul_f32_e32 v9, v83, v9
	v_cvt_pk_bf16_f32 v6, v14, v6
	v_cvt_pk_bf16_f32 v7, v16, v7
	v_mul_f32_e32 v15, v15, v32
	v_mul_f32_e32 v17, v33, v17
	v_cvt_pk_bf16_f32 v8, v15, v8
	v_cvt_pk_bf16_f32 v9, v17, v9
	global_store_dwordx4 v[18:19], v[6:9], off offset:256
	v_mul_f32_e32 v18, 0x3d000000, v80
	v_mul_f32_e32 v17, 0x3d000000, v75
	v_mad_i64_i32 v[6:7], s[22:23], v106, s38, v[12:13]
	v_mul_f32_e32 v8, 0x3d000000, v78
	v_lshl_add_u64 v[14:15], v[6:7], 0, v[10:11]
	v_lshlrev_b32_e32 v6, 16, v20
	v_mul_f32_e32 v6, v8, v6
	v_lshlrev_b32_e32 v8, 16, v21
	v_mul_f32_e32 v9, 0x3d000000, v74
	v_mul_f32_e32 v8, v18, v8
	v_lshlrev_b32_e32 v18, 16, v22
	v_mul_f32_e32 v9, v9, v18
	v_and_b32_e32 v18, 0xffff0000, v22
	v_mul_f32_e32 v16, 0x3d000000, v79
	v_mul_f32_e32 v19, 0x3d000000, v76
	v_and_b32_e32 v7, 0xffff0000, v20
	v_mul_f32_e32 v17, v17, v18
	v_lshlrev_b32_e32 v18, 16, v23
	v_add_co_u32_e32 v14, vcc, s40, v14
	v_mul_f32_e32 v32, 0x3d000000, v81
	v_mul_f32_e32 v33, 0x3d000000, v77
	v_mul_f32_e32 v7, v16, v7
	v_and_b32_e32 v16, 0xffff0000, v21
	v_mul_f32_e32 v18, v19, v18
	v_and_b32_e32 v19, 0xffff0000, v23
	v_cvt_pk_bf16_f32 v6, v6, v7
	v_addc_co_u32_e32 v15, vcc, 0, v15, vcc
	v_mul_f32_e32 v16, v32, v16
	v_mul_f32_e32 v19, v33, v19
	v_cvt_pk_bf16_f32 v7, v8, v16
	v_cvt_pk_bf16_f32 v8, v9, v17
	v_cvt_pk_bf16_f32 v9, v18, v19
	global_store_dwordx4 v[14:15], v[6:9], off
	v_lshlrev_b32_e32 v20, 16, v24
	v_mul_f32_e32 v16, 0x3d000000, v72
	v_mul_f32_e32 v6, 0x3d000000, v70
	v_mul_f32_e32 v8, 0x3d000000, v71
	v_mul_f32_e32 v6, v6, v20
	v_and_b32_e32 v20, 0xffff0000, v24
	v_mul_f32_e32 v8, v8, v20
	v_lshlrev_b32_e32 v20, 16, v25
	v_mul_f32_e32 v18, 0x3d000000, v73
	v_mul_f32_e32 v16, v16, v20
	v_and_b32_e32 v20, 0xffff0000, v25
	v_mul_f32_e32 v7, 0x3d000000, v66
	v_mul_f32_e32 v18, v18, v20
	v_lshlrev_b32_e32 v20, 16, v26
	v_mul_f32_e32 v9, 0x3d000000, v67
	v_mul_f32_e32 v20, v7, v20
	v_and_b32_e32 v7, 0xffff0000, v26
	v_mul_f32_e32 v17, 0x3d000000, v68
	v_mul_f32_e32 v9, v9, v7
	v_lshlrev_b32_e32 v7, 16, v27
	v_mul_f32_e32 v19, 0x3d000000, v69
	v_mul_f32_e32 v17, v17, v7
	v_and_b32_e32 v7, 0xffff0000, v27
	v_mul_f32_e32 v19, v19, v7
	v_cvt_pk_bf16_f32 v6, v6, v8
	v_cvt_pk_bf16_f32 v7, v16, v18
	v_cvt_pk_bf16_f32 v8, v20, v9
	v_cvt_pk_bf16_f32 v9, v17, v19
	global_store_dwordx4 v[14:15], v[6:9], off offset:256
	v_mul_f32_e32 v18, 0x3d000000, v64
	v_mul_f32_e32 v17, 0x3d000000, v59
	v_mad_i64_i32 v[6:7], s[22:23], v107, s38, v[12:13]
	v_mul_f32_e32 v8, 0x3d000000, v62
	v_lshl_add_u64 v[14:15], v[6:7], 0, v[10:11]
	v_lshlrev_b32_e32 v6, 16, v28
	v_mul_f32_e32 v6, v8, v6
	v_lshlrev_b32_e32 v8, 16, v29
	v_mul_f32_e32 v9, 0x3d000000, v58
	v_mul_f32_e32 v8, v18, v8
	v_lshlrev_b32_e32 v18, 16, v30
	v_mul_f32_e32 v9, v9, v18
	v_and_b32_e32 v18, 0xffff0000, v30
	v_mul_f32_e32 v16, 0x3d000000, v63
	v_mul_f32_e32 v19, 0x3d000000, v60
	v_and_b32_e32 v7, 0xffff0000, v28
	v_mul_f32_e32 v17, v17, v18
	v_lshlrev_b32_e32 v18, 16, v31
	v_add_co_u32_e32 v14, vcc, s40, v14
	v_mul_f32_e32 v20, 0x3d000000, v65
	v_mul_f32_e32 v21, 0x3d000000, v61
	v_mul_f32_e32 v7, v16, v7
	v_and_b32_e32 v16, 0xffff0000, v29
	v_mul_f32_e32 v18, v19, v18
	v_and_b32_e32 v19, 0xffff0000, v31
	v_cvt_pk_bf16_f32 v6, v6, v7
	v_addc_co_u32_e32 v15, vcc, 0, v15, vcc
	v_mul_f32_e32 v16, v20, v16
	v_mul_f32_e32 v19, v21, v19
	v_cvt_pk_bf16_f32 v7, v8, v16
	v_cvt_pk_bf16_f32 v8, v9, v17
	v_cvt_pk_bf16_f32 v9, v18, v19
	global_store_dwordx4 v[14:15], v[6:9], off
	v_lshlrev_b32_e32 v20, 16, v98
	v_mul_f32_e32 v16, 0x3d000000, v56
	v_mul_f32_e32 v6, 0x3d000000, v54
	v_mul_f32_e32 v8, 0x3d000000, v55
	v_mul_f32_e32 v6, v6, v20
	v_and_b32_e32 v20, 0xffff0000, v98
	v_mul_f32_e32 v8, v8, v20
	v_lshlrev_b32_e32 v20, 16, v99
	v_mul_f32_e32 v18, 0x3d000000, v57
	v_mul_f32_e32 v16, v16, v20
	v_and_b32_e32 v20, 0xffff0000, v99
	v_mul_f32_e32 v7, 0x3d000000, v50
	v_mul_f32_e32 v18, v18, v20
	v_lshlrev_b32_e32 v20, 16, v100
	v_mul_f32_e32 v9, 0x3d000000, v51
	v_mul_f32_e32 v20, v7, v20
	v_and_b32_e32 v7, 0xffff0000, v100
	v_mul_f32_e32 v17, 0x3d000000, v52
	v_mul_f32_e32 v9, v9, v7
	v_lshlrev_b32_e32 v7, 16, v101
	v_mul_f32_e32 v19, 0x3d000000, v53
	v_mul_f32_e32 v17, v17, v7
	v_and_b32_e32 v7, 0xffff0000, v101
	v_mul_f32_e32 v19, v19, v7
	v_cvt_pk_bf16_f32 v6, v6, v8
	v_cvt_pk_bf16_f32 v7, v16, v18
	v_cvt_pk_bf16_f32 v8, v20, v9
	v_cvt_pk_bf16_f32 v9, v17, v19
	global_store_dwordx4 v[14:15], v[6:9], off offset:256
	v_mul_f32_e32 v14, 0x3d000000, v48
	v_mul_f32_e32 v15, 0x3d000000, v44
	v_mad_i64_i32 v[6:7], s[22:23], v108, s38, v[12:13]
	v_mul_f32_e32 v8, 0x3d000000, v46
	v_lshl_add_u64 v[10:11], v[6:7], 0, v[10:11]
	v_lshlrev_b32_e32 v6, 16, v102
	v_mul_f32_e32 v6, v8, v6
	v_lshlrev_b32_e32 v8, 16, v103
	v_mul_f32_e32 v9, 0x3d000000, v42
	v_mul_f32_e32 v8, v14, v8
	v_lshlrev_b32_e32 v14, 16, v104
	v_mul_f32_e32 v12, 0x3d000000, v47
	v_mul_f32_e32 v13, 0x3d000000, v43
	v_and_b32_e32 v7, 0xffff0000, v102
	v_mul_f32_e32 v9, v9, v14
	v_and_b32_e32 v14, 0xffff0000, v104
	v_mul_f32_e32 v16, 0x3d000000, v49
	v_mul_f32_e32 v7, v12, v7
	v_and_b32_e32 v12, 0xffff0000, v103
	v_mul_f32_e32 v13, v13, v14
	v_lshlrev_b32_e32 v14, 16, v105
	v_add_co_u32_e32 v10, vcc, s40, v10
	v_mul_f32_e32 v17, 0x3d000000, v45
	v_mul_f32_e32 v12, v16, v12
	v_mul_f32_e32 v14, v15, v14
	v_and_b32_e32 v15, 0xffff0000, v105
	v_cvt_pk_bf16_f32 v6, v6, v7
	v_cvt_pk_bf16_f32 v7, v8, v12
	v_cvt_pk_bf16_f32 v8, v9, v13
	v_addc_co_u32_e32 v11, vcc, 0, v11, vcc
	v_mul_f32_e32 v15, v17, v15
	v_cvt_pk_bf16_f32 v9, v14, v15
	global_store_dwordx4 v[10:11], v[6:9], off
	v_lshlrev_b32_e32 v16, 16, v2
	v_and_b32_e32 v2, 0xffff0000, v2
	v_mul_f32_e32 v8, 0x3d000000, v39
	v_mul_f32_e32 v12, 0x3d000000, v40
	v_mul_f32_e32 v2, v8, v2
	v_lshlrev_b32_e32 v8, 16, v3
	v_mul_f32_e32 v9, 0x3d000000, v35
	v_mul_f32_e32 v8, v12, v8
	v_lshlrev_b32_e32 v12, 16, v4
	v_and_b32_e32 v4, 0xffff0000, v4
	v_mul_f32_e32 v14, 0x3d000000, v41
	v_mul_f32_e32 v15, 0x3d000000, v37
	v_and_b32_e32 v3, 0xffff0000, v3
	v_mul_f32_e32 v4, v9, v4
	v_lshlrev_b32_e32 v9, 16, v5
	v_and_b32_e32 v5, 0xffff0000, v5
	v_mul_f32_e32 v6, 0x3d000000, v38
	v_mul_f32_e32 v7, 0x3d000000, v34
	v_mul_f32_e32 v13, 0x3d000000, v36
	v_mul_f32_e32 v3, v14, v3
	v_mul_f32_e32 v5, v15, v5
	s_andn2_b64 vcc, exec, s[0:1]
	s_mov_b64 s[0:1], -1
	v_mul_f32_e32 v6, v6, v16
	v_mul_f32_e32 v7, v7, v12
	v_mul_f32_e32 v9, v13, v9
	v_cvt_pk_bf16_f32 v2, v6, v2
	v_cvt_pk_bf16_f32 v3, v8, v3
	v_cvt_pk_bf16_f32 v4, v7, v4
	v_cvt_pk_bf16_f32 v5, v9, v5
	global_store_dwordx4 v[10:11], v[2:5], off offset:256
	s_cbranch_vccnz .LBB0_984
	s_andn2_b64 vcc, exec, s[6:7]
	s_cbranch_vccnz .LBB0_983
	s_barrier
	s_branch .LBB0_983
